# baseline (speedup 1.0000x reference)
.LBB0_82:
	s_and_b32 s0, s2, 3
	s_lshl_b32 s0, s0, s4
	v_or3_b32 v13, v14, s0, v13
	s_ashr_i32 s0, s2, 1
	s_and_b32 s0, s0, -16
	v_lshrrev_b32_e32 v11, 3, v0
	v_lshl_add_u32 v13, v13, 7, s0
	v_and_or_b32 v14, v11, 15, v13
	v_mov_b32_e32 v16, s16
	v_mov_b32_e32 v17, s17
	v_ashrrev_i32_e32 v15, 31, v14
	v_lshl_add_u64 v[14:15], v[14:15], 2, v[16:17]
	global_load_dword v13, v[14:15], off
	s_lshl_b32 s4, s33, 5
	v_cmp_gt_u32_e32 vcc, 32, v0
	s_and_saveexec_b64 s[0:1], vcc
	v_mov_b32_e32 v14, 0x14a00
	v_lshl_add_u32 v14, v0, 2, v14
	v_mov_b32_e32 v15, 0
	ds_write_b32 v14, v15
	s_or_b64 exec, exec, s[0:1]
	v_mov_b32_e32 v49, 0
	v_lshlrev_b32_e32 v48, 4, v0
	v_lshl_add_u64 v[14:15], s[34:35], 0, v[48:49]
	v_add_co_u32_e32 v28, vcc, 0x2000, v14
	global_load_dwordx4 v[16:19], v48, s[34:35]
	s_nop 0
	v_addc_co_u32_e32 v29, vcc, 0, v15, vcc
	v_add_co_u32_e32 v30, vcc, 0x4000, v14
	s_mov_b32 s1, 0
	s_nop 0
	v_addc_co_u32_e32 v31, vcc, 0, v15, vcc
	v_add_co_u32_e32 v14, vcc, 0x6000, v14
	global_load_dwordx4 v[20:23], v[28:29], off
	global_load_dwordx4 v[24:27], v[30:31], off
	v_addc_co_u32_e32 v15, vcc, 0, v15, vcc
	global_load_dwordx4 v[28:31], v[14:15], off
	v_lshlrev_b32_e32 v14, 6, v0
	v_and_b32_e32 v14, 0x7e00, v14
	v_mov_b32_e32 v15, v49
	v_lshl_add_u64 v[32:33], s[18:19], 0, v[14:15]
	s_lshl_b32 s0, s4, 2
	v_lshl_add_u64 v[32:33], v[32:33], 0, s[0:1]
	v_and_b32_e32 v44, 0x70, v48
	v_mov_b32_e32 v45, v49
	v_lshl_add_u64 v[32:33], v[32:33], 0, v[44:45]
	v_or_b32_e32 v46, 0x8000, v14
	v_mov_b32_e32 v47, v49
	global_load_dwordx4 v[32:35], v[32:33], off
	v_lshl_add_u64 v[36:37], s[18:19], 0, v[46:47]
	v_lshl_add_u64 v[14:15], s[22:23], 0, v[14:15]
	v_lshl_add_u64 v[36:37], v[36:37], 0, s[0:1]
	v_lshl_add_u64 v[14:15], v[14:15], 0, s[0:1]
	v_lshl_add_u64 v[36:37], v[36:37], 0, v[44:45]
	v_lshl_add_u64 v[14:15], v[14:15], 0, v[44:45]
	global_load_dwordx4 v[36:39], v[36:37], off
	v_lshlrev_b32_e32 v49, 3, v0
	global_load_dwordx4 v[40:43], v[14:15], off
	v_lshl_add_u64 v[14:15], s[22:23], 0, v[46:47]
	v_lshl_add_u64 v[14:15], v[14:15], 0, s[0:1]
	v_lshl_add_u64 v[14:15], v[14:15], 0, v[44:45]
	global_load_dwordx4 v[44:47], v[14:15], off
	v_lshrrev_b32_e32 v50, 1, v0
	v_lshrrev_b32_e32 v15, 5, v0
	v_and_b32_e32 v14, 4, v0
	v_lshrrev_b32_e32 v52, 2, v0
	v_lshrrev_b32_e32 v53, 8, v0
	v_and_b32_e32 v48, 48, v48
	v_and_b32_e32 v49, 0xc0, v49
	v_and_b32_e32 v50, 48, v50
	v_lshrrev_b32_e32 v51, 4, v0
	v_lshlrev_b32_e32 v54, 1, v14
	v_and_b32_e32 v52, 6, v52
	v_or_b32_e32 v53, v53, v14
	v_or3_b32 v15, v48, v15, v49
	v_and_or_b32 v48, v10, 12, v50
	v_and_or_b32 v49, v51, 8, v52
	v_lshlrev_b32_e32 v50, 10, v53
	v_lshl_or_b32 v15, v15, 4, v54
	v_lshlrev_b32_e32 v48, 4, v48
	v_or3_b32 v48, v50, v48, v49
	v_add_u32_e32 v48, 0x10a00, v48
	s_movk_i32 s0, 0x80
	v_cmp_gt_u32_e32 vcc, s0, v0
	s_waitcnt vmcnt(7)
	v_cvt_pk_f16_f32 v16, v16, v17
	v_cvt_pk_f16_f32 v17, v18, v19
	s_waitcnt vmcnt(6)
	v_cvt_pk_f16_f32 v18, v20, v21
	v_cvt_pk_f16_f32 v19, v22, v23
	ds_write2st64_b64 v15, v[16:17], v[18:19] offset0:101 offset1:109
	s_waitcnt vmcnt(5)
	v_cvt_pk_f16_f32 v16, v24, v25
	v_cvt_pk_f16_f32 v17, v26, v27
	s_waitcnt vmcnt(4)
	v_cvt_pk_f16_f32 v18, v28, v29
	v_cvt_pk_f16_f32 v19, v30, v31
	s_waitcnt vmcnt(3)
	v_cvt_f16_f32_e32 v20, v32
	v_cvt_f16_f32_e32 v21, v33
	v_cvt_f16_f32_e32 v22, v34
	v_cvt_f16_f32_e32 v23, v35
	s_waitcnt vmcnt(2)
	v_cvt_f16_f32_e32 v24, v36
	v_cvt_f16_f32_e32 v25, v37
	v_cvt_f16_f32_e32 v26, v38
	v_cvt_f16_f32_e32 v27, v39
	ds_write2st64_b64 v15, v[16:17], v[18:19] offset0:117 offset1:125
	ds_write_b16 v48, v20
	ds_write_b16 v48, v21 offset:16
	ds_write_b16 v48, v22 offset:32
	ds_write_b16 v48, v23 offset:48
	ds_write_b16 v48, v24 offset:2048
	ds_write_b16 v48, v25 offset:2064
	ds_write_b16 v48, v26 offset:2080
	ds_write_b16 v48, v27 offset:2096
	s_waitcnt vmcnt(1)
	v_cvt_f16_f32_e32 v15, v40
	v_cvt_f16_f32_e32 v16, v41
	v_cvt_f16_f32_e32 v17, v42
	v_cvt_f16_f32_e32 v18, v43
	ds_write_b16 v48, v15 offset:8192
	ds_write_b16 v48, v16 offset:8208
	ds_write_b16 v48, v17 offset:8224
	ds_write_b16 v48, v18 offset:8240
	s_waitcnt vmcnt(0)
	v_cvt_f16_f32_e32 v15, v44
	v_cvt_f16_f32_e32 v16, v45
	v_cvt_f16_f32_e32 v17, v46
	v_cvt_f16_f32_e32 v18, v47
	ds_write_b16 v48, v15 offset:10240
	ds_write_b16 v48, v16 offset:10256
	ds_write_b16 v48, v17 offset:10272
	ds_write_b16 v48, v18 offset:10288
	s_and_saveexec_b64 s[0:1], vcc
	s_cbranch_execz .LBB0_86
	v_cvt_f16_f32_e32 v13, v13
	v_lshl_or_b32 v18, s2, 7, v0
	v_mov_b32_e32 v16, s28
	v_mov_b32_e32 v17, s29
	v_ashrrev_i32_e32 v19, 31, v18
	v_lshl_add_u64 v[16:17], v[18:19], 1, v[16:17]
	global_store_short v[16:17], v13, off sc0 sc1
